# neighbourhood-attention background conversion step (now layer 0 only) runs on every second 2-tile iteration
# speedup vs baseline: 1.0159x; 1.0029x over previous
.LBB0_253:
	s_cmp_lt_i32 s30, 4
	s_cselect_b64 s[8:9], -1, 0
	s_and_b64 s[4:5], s[8:9], s[4:5]
	s_andn2_b64 vcc, exec, s[4:5]
	s_cbranch_vccnz .LBB0_364
	s_mov_b64 s[10:11], s[0:1]
	s_mov_b32 s98, 0x18000
	s_cmpk_eq_u32 s22, 0x100
	s_cselect_b32 s98, 0xc000, s98
	s_mov_b32 s99, 0
	s_load_dwordx2 s[4:5], s[10:11], 0xd8
	v_readlane_b32 s12, v255, 6
	s_mul_i32 s6, s12, 0x2080
	v_mbcnt_hi_u32_b32 v4, -1, v208
	s_add_i32 s6, s6, 0
	s_waitcnt lgkmcnt(0)
	s_add_u32 s23, s4, 0x11800000
	v_lshlrev_b32_e32 v2, 2, v4
	v_and_b32_e32 v210, 60, v2
	v_lshlrev_b32_e32 v2, 3, v4
	s_addc_u32 s26, s5, 0
	v_and_b32_e32 v194, 24, v2
	v_ashrrev_i32_e32 v211, 2, v4
	s_add_u32 s27, s4, 0x1800000
	v_ashrrev_i32_e32 v209, 4, v4
	s_movk_i32 s7, 0x104
	v_mul_u32_u24_e32 v2, 0x104, v194
	v_mov_b32_e32 v3, 0
	v_and_b32_e32 v5, -4, v4
	v_add_u32_e32 v213, 16, v211
	v_add_u32_e32 v215, 32, v211
	v_add_u32_e32 v217, 48, v211
	s_addc_u32 s35, s5, 0
	s_mov_b32 s65, 0
	v_lshl_add_u32 v220, v210, 2, s6
	v_mul_lo_u32 v221, v209, s7
	v_mov_b32_e32 v195, v3
	v_add3_u32 v219, s6, v2, v5
	v_ashrrev_i32_e32 v212, 31, v211
	v_ashrrev_i32_e32 v214, 31, v213
	v_ashrrev_i32_e32 v216, 31, v215
	s_cmpk_gt_i32 s88, 0x81f
	v_ashrrev_i32_e32 v218, 31, v217
	s_cbranch_scc1 .LBB0_352
	s_add_u32 s15, s4, 0x25b00000
	s_addc_u32 s48, s5, 0
	s_add_u32 s49, s4, 0x29c00000
	s_addc_u32 s50, s5, 0
	s_add_u32 s51, s4, 0x2dd00000
	s_addc_u32 s53, s5, 0
	v_and_b32_e32 v2, 31, v4
	v_ashrrev_i32_e32 v4, 3, v4
	s_lshl_b32 s54, s12, 5
	s_lshr_b32 s55, s3, 7
	v_and_b32_e32 v222, -4, v4
	v_lshl_add_u64 v[4:5], s[4:5], 0, v[2:3]
	s_mov_b64 s[4:5], 0x31e00000
	v_and_or_b32 v2, s54, 32, v2
	s_cmp_lg_u32 0, -1
	v_lshl_add_u64 v[196:197], v[4:5], 0, s[4:5]
	v_sub_u32_e64 v4, v2, 8 clamp
	s_cselect_b32 s4, 0, 0
	s_and_b32 s3, s3, 0xffffff80
	v_min_u32_e32 v223, 48, v4
	s_sub_i32 s3, s4, s3
	v_sub_u32_e32 v224, 15, v2
	v_add_u32_e32 v225, 16, v223
	s_mov_b32 s13, 0
	s_add_i32 s3, s3, 0x8800
	s_mov_b64 s[20:21], 0
	s_mov_b64 s[18:19], 0
	s_mov_b32 s56, 0x41000000
	s_mov_b32 s14, 0x42000000
	s_movk_i32 s57, 0x1e0
	s_movk_i32 s58, 0xffdf
	s_add_i32 s59, 0, 0x4000
	s_mov_b32 s60, s88
	s_mov_b32 s61, s88
	s_mov_b32 s63, 0
	s_mov_b32 s62, s52
	s_cmpk_gt_i32 s61, 0x7ff
	s_mov_b64 s[4:5], -1
	s_cbranch_scc0 .LBB0_290
	s_branch .LBB0_257

.LBB0_321:
	s_andn2_b64 vcc, exec, s[20:21]
	s_waitcnt lgkmcnt(0)
	s_barrier
	s_xor_b32 s99, s99, 1
	s_cmp_lg_u32 s99, 0
	s_cbranch_scc1 .LBB0_329
	s_cbranch_vccnz .LBB0_323
	v_add_u32_e32 v2, v220, v221
	v_pk_mul_f32 v[52:53], v[98:99], s[14:15] op_sel_hi:[1,0]
	v_add_u32_e32 v54, 0x9000, v2
	ds_write2_b32 v54, v52, v53 offset1:1
	v_pk_mul_f32 v[52:53], v[100:101], s[14:15] op_sel_hi:[1,0]
	v_add_u32_e32 v54, 0x9008, v2
	ds_write2_b32 v54, v52, v53 offset1:1
	v_pk_mul_f32 v[52:53], v[102:103], s[14:15] op_sel_hi:[1,0]
	v_add_u32_e32 v54, 0x9410, v2
	ds_write2_b32 v54, v52, v53 offset1:1
	v_pk_mul_f32 v[52:53], v[104:105], s[14:15] op_sel_hi:[1,0]
	v_add_u32_e32 v54, 0x9418, v2
	ds_write2_b32 v54, v52, v53 offset1:1
	v_pk_mul_f32 v[52:53], v[106:107], s[14:15] op_sel_hi:[1,0]
	v_add_u32_e32 v54, 0x9820, v2
	ds_write2_b32 v54, v52, v53 offset1:1
	v_pk_mul_f32 v[52:53], v[108:109], s[14:15] op_sel_hi:[1,0]
	v_add_u32_e32 v54, 0x9828, v2
	ds_write2_b32 v54, v52, v53 offset1:1
	v_pk_mul_f32 v[52:53], v[110:111], s[14:15] op_sel_hi:[1,0]
	v_add_u32_e32 v54, 0x9c30, v2
	ds_write2_b32 v54, v52, v53 offset1:1
	v_pk_mul_f32 v[52:53], v[112:113], s[14:15] op_sel_hi:[1,0]
	v_add_u32_e32 v54, 0x9c38, v2
	ds_write2_b32 v54, v52, v53 offset1:1
	v_pk_mul_f32 v[52:53], v[114:115], s[14:15] op_sel_hi:[1,0]
	v_add_u32_e32 v54, 0xa040, v2
	ds_write2_b32 v54, v52, v53 offset1:1
	v_pk_mul_f32 v[52:53], v[116:117], s[14:15] op_sel_hi:[1,0]
	v_add_u32_e32 v54, 0xa048, v2
	ds_write2_b32 v54, v52, v53 offset1:1
	v_pk_mul_f32 v[52:53], v[118:119], s[14:15] op_sel_hi:[1,0]
	v_add_u32_e32 v54, 0xa450, v2
	ds_write2_b32 v54, v52, v53 offset1:1
	v_pk_mul_f32 v[52:53], v[120:121], s[14:15] op_sel_hi:[1,0]
	v_add_u32_e32 v54, 0xa458, v2
	ds_write2_b32 v54, v52, v53 offset1:1
	v_pk_mul_f32 v[52:53], v[122:123], s[14:15] op_sel_hi:[1,0]
	v_add_u32_e32 v54, 0xa860, v2
	ds_write2_b32 v54, v52, v53 offset1:1
	v_pk_mul_f32 v[52:53], v[124:125], s[14:15] op_sel_hi:[1,0]
	v_add_u32_e32 v54, 0xa868, v2
	ds_write2_b32 v54, v52, v53 offset1:1
	v_pk_mul_f32 v[52:53], v[126:127], s[14:15] op_sel_hi:[1,0]
	v_add_u32_e32 v54, 0xac70, v2
	ds_write2_b32 v54, v52, v53 offset1:1
	v_pk_mul_f32 v[52:53], v[128:129], s[14:15] op_sel_hi:[1,0]
	v_add_u32_e32 v2, 0xac78, v2
	ds_write2_b32 v2, v52, v53 offset1:1
	s_waitcnt lgkmcnt(0)
	v_add_u32_e32 v76, 0x9000, v219
	ds_read2_b32 v[52:53], v76 offset1:16
	ds_read2_b32 v[54:55], v76 offset0:65 offset1:81
	v_add_u32_e32 v77, 0x9400, v219
	ds_read2_b32 v[58:59], v76 offset0:130 offset1:146
	ds_read2_b32 v[60:61], v77 offset0:4 offset1:20
	ds_read2_b32 v[62:63], v77 offset0:69 offset1:85
	ds_read2_b32 v[64:65], v76 offset0:195 offset1:211
	v_mov_b32_e32 v56, v3
	v_mov_b32_e32 v57, v3
	ds_read2_b32 v[66:67], v77 offset0:134 offset1:150
	ds_read2_b32 v[68:69], v77 offset0:199 offset1:215
	s_waitcnt lgkmcnt(6)
	v_cvt_pk_fp8_f32 v56, v52, v54
	s_waitcnt lgkmcnt(3)
	v_cvt_pk_fp8_f32 v57, v60, v62
	v_mov_b64_e32 v[70:71], s[18:19]
	v_mad_u64_u32 v[72:73], s[20:21], s63, v211, v[70:71]
	s_waitcnt lgkmcnt(2)
	v_cvt_pk_fp8_f32 v56, v58, v64 op_sel:[0,0,1]
	s_waitcnt lgkmcnt(0)
	v_cvt_pk_fp8_f32 v57, v66, v68 op_sel:[0,0,1]
	v_mov_b32_e32 v2, v73
	v_mov_b32_e32 v52, v3
	v_mad_u64_u32 v[74:75], s[20:21], s63, v212, v[2:3]
	v_cvt_pk_fp8_f32 v52, v53, v55
	v_mov_b32_e32 v53, v3
	v_mov_b32_e32 v73, v74
	v_cvt_pk_fp8_f32 v53, v61, v63
	v_lshl_add_u64 v[54:55], v[72:73], 0, v[194:195]
	global_store_dwordx2 v[54:55], v[56:57], off
	v_cvt_pk_fp8_f32 v52, v59, v65 op_sel:[0,0,1]
	ds_read2_b32 v[56:57], v76 offset0:32 offset1:48
	ds_read2_b32 v[58:59], v76 offset0:97 offset1:113
	v_cvt_pk_fp8_f32 v53, v67, v69 op_sel:[0,0,1]
	v_mad_u64_u32 v[54:55], s[20:21], s63, v213, v[70:71]
	ds_read2_b32 v[62:63], v76 offset0:162 offset1:178
	ds_read2_b32 v[64:65], v77 offset0:36 offset1:52
	ds_read2_b32 v[66:67], v77 offset0:101 offset1:117
	ds_read2_b32 v[68:69], v76 offset0:227 offset1:243
	v_mov_b32_e32 v2, v55
	v_mad_u64_u32 v[60:61], s[20:21], s63, v214, v[2:3]
	v_mov_b32_e32 v55, v60
	v_mov_b32_e32 v60, v3
	v_mov_b32_e32 v61, v3
	ds_read2_b32 v[72:73], v77 offset0:166 offset1:182
	ds_read2_b32 v[74:75], v77 offset0:231 offset1:247
	s_waitcnt lgkmcnt(6)
	v_cvt_pk_fp8_f32 v60, v56, v58
	s_waitcnt lgkmcnt(3)
	v_cvt_pk_fp8_f32 v61, v64, v66
	v_lshl_add_u64 v[54:55], v[54:55], 0, v[194:195]
	global_store_dwordx2 v[54:55], v[52:53], off
	v_mad_u64_u32 v[52:53], s[20:21], s63, v215, v[70:71]
	v_mov_b32_e32 v2, v53
	v_mad_u64_u32 v[54:55], s[20:21], s63, v216, v[2:3]
	s_waitcnt lgkmcnt(2)
	v_cvt_pk_fp8_f32 v60, v62, v68 op_sel:[0,0,1]
	s_waitcnt lgkmcnt(0)
	v_cvt_pk_fp8_f32 v61, v72, v74 op_sel:[0,0,1]
	v_mov_b32_e32 v53, v54
	v_mov_b32_e32 v54, v3
	v_mov_b32_e32 v55, v3
	v_cvt_pk_fp8_f32 v54, v57, v59
	v_cvt_pk_fp8_f32 v55, v65, v67
	v_lshl_add_u64 v[52:53], v[52:53], 0, v[194:195]
	global_store_dwordx2 v[52:53], v[60:61], off
	v_mad_u64_u32 v[52:53], s[20:21], s63, v217, v[70:71]
	v_cvt_pk_fp8_f32 v54, v63, v69 op_sel:[0,0,1]
	v_cvt_pk_fp8_f32 v55, v73, v75 op_sel:[0,0,1]
	v_mov_b32_e32 v2, v53
	v_mad_u64_u32 v[56:57], s[20:21], s63, v218, v[2:3]
	v_mov_b32_e32 v53, v56
	v_lshl_add_u64 v[52:53], v[52:53], 0, v[194:195]
	global_store_dwordx2 v[52:53], v[54:55], off
	s_waitcnt lgkmcnt(0)
